# v15: P2/P9 - surplus workgroups (52/45 of 256) skip the GEMM and convert expert weights for the whole phase instead of all idle workgroups converting in a burst at the end
# baseline (speedup 1.0000x reference)
; #define SLACK(k) do { __syncthreads(); unsigned* dn_ = (unsigned*)(ws + WS_CTL) + CW_PHDONE + 64 * (k); if (tid_opaque() == 0) __hip_atomic_fetch_add(dn_, 1u, __ATOMIC_RELAXED, __HIP_MEMORY_SCOPE_AGENT); \
;         tr_slack(P, lds, (unsigned*)(ws + WS_CTL) + CW_TILE, dn_, (unsigned)G); } while (0)
;     __device__ __forceinline__ bool next(int i, Unit& u) const {
;         const int L = i * G + c; const int n0 = nM0 * nN0;
;         if (L < n0) { tile_map(L, nM0, nN0, u.pm, u.pn); u.g = -1; u.kt0 = 0; u.nt = ntK; }
;         else { const int l2 = L - n0; if (l2 >= nM1 * nN1 * ksplit) return false; int a, b; const int part = l2 % ksplit; tile_map(l2 / ksplit, nM1, nN1, a, b); u.pm = pm1 + a; u.pn = pn1 + b;
;             if (ksplit > 1) { u.g = part; u.nt = ntK / ksplit; u.kt0 = part * u.nt; } else { u.g = -1; u.kt0 = 0; u.nt = ntK; } }
;         u.orow0 = u.pm * BM; return true;
; __global__ void __launch_bounds__(512, 2) fwd_kernel(Params KP) {
;     ...
;         pg8::DenseSched S{(const char*)(ws + WS_WEIN), DM / 2, DM / 2, G, bx, MT / 256, 12, 0, 0, 0, 0, DM / 128, 1};
;         pg8::EpiEIn E{(bf16_t*)(ws + WS_U), (bf16_t*)(ws + WS_Z), (const float*)(ws + WS_RSC), ctlf + CW_CMAX_EIN};
;         pg8::gemm_phase<pg8::EpiEIn, pg8::DenseSched, 2>(lds, (const char*)(ws + WS_HN), DM / 2, S, E);
;         SLACK(2);
.LBB0_558:
	s_or_b64 exec, exec, s[40:41]
	s_mov_b64 s[2:3], s[0:1]
	s_nop 0
	v_mov_b64_e32 v[2:3], s[2:3]
	flat_load_dword v1, v[2:3] offset:296
	s_waitcnt vmcnt(0) lgkmcnt(0)
	v_cmp_gt_i32_e32 vcc, 3, v1
	s_and_saveexec_b64 s[10:11], vcc
	s_cbranch_execz .LBB0_613
	s_mov_b64 s[2:3], s[0:1]
	s_nop 0
	v_mov_b64_e32 v[2:3], s[2:3]
	flat_load_dword v1, v[2:3] offset:300
	s_waitcnt vmcnt(0) lgkmcnt(0)
	v_cmp_lt_i32_e32 vcc, 2, v1
	s_and_b64 exec, exec, vcc
	s_cbranch_execz .LBB0_613
	s_cmp_eq_u32 s39, 0x100
	s_cselect_b32 s99, 204, s39
	s_cmp_lt_u32 s8, s99
	s_cselect_b32 s98, s8, 0x7fff
	s_mov_b64 s[12:13], s[0:1]
	s_mov_b64 s[2:3], s[0:1]
	v_readfirstlane_b32 s25, v0
	v_lshlrev_b32_e32 v168, 4, v0
	v_lshrrev_b32_e32 v169, 5, v0
	s_cmpk_gt_i32 s98, 0x32f
	v_lshrrev_b32_e32 v1, 3, v0
	s_cbranch_scc1 .LBB0_585
	v_and_b32_e32 v2, 32, v0
	v_bitop3_b32 v2, v168, v2, 48 bitop3:0x6c
	v_and_or_b32 v170, v0, 64, v2
	v_lshrrev_b32_e32 v2, 1, v0
	v_and_b32_e32 v2, 24, v2
	v_and_b32_e32 v4, 4, v169
	v_bfe_u32 v5, v0, 2, 2
	v_or3_b32 v4, v4, v5, v2
	v_and_or_b32 v5, v1, 32, v4
	s_add_u32 s9, s36, 0x400000
	v_lshl_or_b32 v172, v5, 11, v170
	v_or_b32_e32 v5, 0x2000, v168
	s_addc_u32 s27, s37, 0
	v_bfe_u32 v3, v0, 2, 4
	v_lshrrev_b32_e32 v5, 7, v5
	s_movk_i32 s4, 0x70
	s_add_u32 s2, s36, 0x24ac0000
	v_and_or_b32 v173, v5, s4, v3
	s_movk_i32 s4, 0x60
	s_addc_u32 s3, s37, 0
	v_and_or_b32 v171, v1, 48, v3
	v_and_or_b32 v3, v5, s4, v4
	s_ashr_i32 s4, s98, 31
	s_lshr_b32 s4, s4, 29
	s_add_i32 s4, s98, s4
	s_lshr_b32 s20, s25, 6
	s_and_b32 s5, s4, -8
	s_lshr_b32 s26, s25, 8
	s_lshl_b32 s38, s20, 10
	s_sub_i32 s5, s98, s5
	s_cmp_lt_i32 s5, 0
	s_movk_i32 s60, 0x67
	s_cselect_b32 s6, s60, 0x66
	s_mul_i32 s5, s5, s6
	s_ashr_i32 s4, s4, 3
	s_add_i32 s5, s5, s4
	s_mul_hi_i32 s4, s5, 0x2aaaaaab
	s_lshr_b32 s6, s4, 31
	s_ashr_i32 s4, s4, 4
	s_add_i32 s4, s4, s6
	s_lshl_b32 s6, s4, 3
	s_sub_i32 s7, 0x44, s6
	s_mulk_i32 s4, 0x60
	s_min_u32 s7, s7, 8
	s_sub_i32 s14, s5, s4
	s_sext_i32_i8 s4, s14
	v_cvt_f32_ubyte0_e32 v5, s7
	v_cvt_f32_i32_e32 v4, s4
	v_rcp_iflag_f32_e32 v6, v5
	v_lshl_or_b32 v174, v3, 11, v170
	s_ashr_i32 s4, s4, 30
	s_or_b32 s15, s4, 1
	v_mul_f32_e32 v3, v4, v6
	v_trunc_f32_e32 v3, v3
	v_fma_f32 v4, -v3, v5, v4
	v_cvt_i32_f32_e32 v3, v3
	v_cmp_ge_f32_e64 s[4:5], |v4|, v5
	s_and_b64 s[4:5], s[4:5], exec
	s_cselect_b32 s4, s15, 0
	v_readfirstlane_b32 s5, v3
	s_add_i32 s24, s5, s4
	s_mul_i32 s4, s24, s7
	s_sub_i32 s4, s14, s4
	s_sext_i32_i8 s4, s4
	s_add_i32 s6, s6, s4
	s_lshl_b32 s81, s6, 8
	v_or_b32_e32 v3, s81, v171
	v_lshl_or_b32 v175, v3, 11, v170
	v_or_b32_e32 v3, s81, v173
	s_or_b32 s4, s81, 0x80
	v_lshl_or_b32 v176, v3, 11, v170
	v_or_b32_e32 v3, s4, v171
	v_lshl_or_b32 v177, v3, 11, v170
	v_or_b32_e32 v3, s4, v173
	s_bfe_i64 s[4:5], s[24:25], 0x80000
	s_lshl_b64 s[4:5], s[4:5], 19
	s_add_u32 s52, s9, s4
	s_addc_u32 s53, s27, s5
	s_add_i32 s61, s38, 0
	v_lshl_or_b32 v178, v3, 11, v170
	s_add_i32 s62, s61, 0x10000
	v_mov_b32_e32 v3, v172
	s_mov_b32 m0, s62
	s_add_i32 s63, s61, 0x12000
	global_load_lds_dwordx4 v3, s[52:53]
	v_mov_b32_e32 v3, v174
	s_mov_b32 m0, s63
	s_add_u32 s4, s52, 0x40000
	global_load_lds_dwordx4 v3, s[52:53]
	s_addc_u32 s5, s53, 0
	s_add_i32 s64, s61, 0x14000
	v_mov_b32_e32 v3, v172
	s_mov_b32 m0, s64
	s_add_i32 s65, s61, 0x16000
	global_load_lds_dwordx4 v3, s[4:5]
	v_mov_b32_e32 v3, v174
	s_mov_b32 m0, s65
	s_add_i32 s66, s61, 0x2000
	global_load_lds_dwordx4 v3, s[4:5]
	v_mov_b32_e32 v3, v175
	s_mov_b32 m0, s61
	s_add_i32 s67, s61, 0x4000
	global_load_lds_dwordx4 v3, s[2:3]
	v_mov_b32_e32 v3, v176
	s_mov_b32 m0, s66
	s_add_i32 s68, s61, 0x6000
	global_load_lds_dwordx4 v3, s[2:3]
	v_mov_b32_e32 v3, v177
	s_mov_b32 m0, s67
	s_cmp_eq_u32 s26, 1
	global_load_lds_dwordx4 v3, s[2:3]
	v_mov_b32_e32 v3, v178
	s_mov_b32 m0, s68
	s_mov_b32 s69, 0
	global_load_lds_dwordx4 v3, s[2:3]
	s_mov_b32 s70, 0x10000
	s_cselect_b64 s[4:5], -1, 0
	s_cmp_lg_u32 s26, 1
	s_mov_b64 s[6:7], 0x40000
	s_cbranch_scc1 .LBB0_563
	s_barrier

;     __device__ __forceinline__ bool next(int i, Unit& u) const {
;         const int L = i * G + c; const int n0 = nM0 * nN0;
;         if (L < n0) { tile_map(L, nM0, nN0, u.pm, u.pn); u.g = -1; u.kt0 = 0; u.nt = ntK; }
.LBB0_566:
	s_add_i32 s69, s69, 1
	s_mul_i32 s47, s69, s99
	s_add_i32 s47, s47, s98
	s_cmpk_lt_i32 s47, 0x330
	s_cselect_b64 s[48:49], -1, 0
	s_mov_b64 s[50:51], -1
	s_and_b64 vcc, exec, s[48:49]
	s_cbranch_vccnz .LBB0_568
	s_lshl_b32 s54, s79, 8
	s_mov_b64 s[50:51], 0

; #define SLACK(k) do { __syncthreads(); unsigned* dn_ = (unsigned*)(ws + WS_CTL) + CW_PHDONE + 64 * (k); if (tid_opaque() == 0) __hip_atomic_fetch_add(dn_, 1u, __ATOMIC_RELAXED, __HIP_MEMORY_SCOPE_AGENT); \
;         tr_slack(P, lds, (unsigned*)(ws + WS_CTL) + CW_TILE, dn_, (unsigned)G); } while (0)
;     __device__ __forceinline__ bool next(int i, Unit& u) const {
;         const int L = i * G + c; const int n0 = nM0 * nN0;
;         if (L < n0) { tile_map(L, nM0, nN0, u.pm, u.pn); u.g = -1; u.kt0 = 0; u.nt = ntK; }
;         else { const int l2 = L - n0; if (l2 >= nM1 * nN1 * ksplit) return false; int a, b; const int part = l2 % ksplit; tile_map(l2 / ksplit, nM1, nN1, a, b); u.pm = pm1 + a; u.pn = pn1 + b;
;             if (ksplit > 1) { u.g = part; u.nt = ntK / ksplit; u.kt0 = part * u.nt; } else { u.g = -1; u.kt0 = 0; u.nt = ntK; } }
;         u.orow0 = u.pm * BM; return true;
; __global__ void __launch_bounds__(512, 2) fwd_kernel(Params KP) {
;     ...
;         pg8::DenseSched S{(const char*)(ws + WS_WOIN), DM / 2, DM / 2, G, bx, ML / 256, 13, MC / 256, 3, ML / 256, 2, DM / 128, 1};
;         pg8::EpiOIn E{(bf16_t*)(ws + WS_CQ), (bf16_t*)(ws + WS_CKV), (bf16_t*)(ws + WS_GU), (bf16_t*)(ws + WS_GV), ws + WS_K, ctlf + CW_SSQQ, ctlf + CW_SSQKV, ctlf + CW_ZS1, ctlf + CW_ZS2, (const float*)(ws + WS_ROPE), (const float*)(ws + WS_RSC), ctlf + CW_CMAX_OIN};
;         pg8::gemm_phase<pg8::EpiOIn, pg8::DenseSched, 2>(lds, (const char*)(ws + WS_HN), DM / 2, S, E);
;         SLACK(9);
.LBB0_1729:
	s_or_b64 exec, exec, s[40:41]
	s_mov_b64 s[2:3], s[0:1]
	s_nop 0
	v_mov_b64_e32 v[2:3], s[2:3]
	flat_load_dword v1, v[2:3] offset:296
	s_waitcnt vmcnt(0) lgkmcnt(0)
	v_cmp_gt_i32_e32 vcc, 10, v1
	s_and_saveexec_b64 s[10:11], vcc
	s_cbranch_execz .LBB0_1900
	s_mov_b64 s[2:3], s[0:1]
	s_nop 0
	v_mov_b64_e32 v[2:3], s[2:3]
	flat_load_dword v1, v[2:3] offset:300
	s_waitcnt vmcnt(0) lgkmcnt(0)
	v_cmp_lt_i32_e32 vcc, 9, v1
	s_and_b64 exec, exec, vcc
	s_cbranch_execz .LBB0_1900
	s_cmp_eq_u32 s39, 0x100
	s_cselect_b32 s99, 211, s39
	s_cmp_lt_u32 s8, s99
	s_cselect_b32 s98, s8, 0x7fff
	s_mov_b64 s[12:13], s[0:1]
	s_mov_b64 s[2:3], s[0:1]
	s_cmpk_gt_i32 s98, 0x33f
	v_readfirstlane_b32 s6, v0
	s_cbranch_scc0 .LBB0_1734
	s_add_i32 s4, s98, 0xfffffcc0
	s_cmp_lt_u32 s4, 12
	s_mov_b64 s[2:3], 0
	s_cbranch_scc0 .LBB0_1735
	s_add_i32 s5, s98, 0xfffffcb8
	s_cmp_lt_u32 s4, 8
	s_cselect_b32 s5, s4, s5
	s_lshl_b32 s7, s5, 1
	s_add_i32 s9, s5, 4
	s_cmp_lt_u32 s5, 4
	s_cselect_b32 s7, s7, s9
	s_cmp_gt_u32 s4, 7
	s_cselect_b64 s[4:5], -1, 0
	s_cmp_lg_u64 s[4:5], 0
	s_addc_u32 s4, s7, 0
	s_and_b32 s5, s4, 3
	s_bfe_u32 s4, s4, 0x60002
	s_or_b32 s7, s5, 64
	s_add_i32 s60, s4, 2
	s_mov_b64 s[4:5], -1
	s_and_b64 vcc, exec, s[2:3]
	s_cbranch_vccnz .LBB0_1736
	s_branch .LBB0_1737

;     __device__ __forceinline__ bool next(int i, Unit& u) const {
;     ...
;         if (L < n0) { tile_map(L, nM0, nN0, u.pm, u.pn); u.g = -1; u.kt0 = 0; u.nt = ntK; }
.LBB0_1736:
	s_ashr_i32 s2, s98, 31
	s_lshr_b32 s2, s2, 29
	s_add_i32 s2, s98, s2
	s_and_b32 s3, s2, -8
	s_sub_i32 s3, s98, s3
	s_cmp_lt_i32 s3, 0
	s_movk_i32 s4, 0x69
	s_cselect_b32 s4, s4, 0x68
	s_mul_i32 s3, s3, s4
	s_ashr_i32 s2, s2, 3
	s_add_i32 s3, s3, s2
	s_mul_hi_i32 s2, s3, 0x4ec4ec4f
	s_lshr_b32 s4, s2, 31
	s_ashr_i32 s2, s2, 5
	s_add_i32 s2, s2, s4
	s_lshl_b32 s4, s2, 3
	s_mulk_i32 s2, 0x68
	s_sub_i32 s2, s3, s2
	s_bfe_i32 s3, s2, 0x80000
	s_bfe_u32 s3, s3, 0x3000c
	s_add_i32 s3, s2, s3
	s_bfe_i32 s5, s3, 0x80000
	s_and_b32 s3, s3, 0xf8
	s_sub_i32 s2, s2, s3
	s_sext_i32_i16 s5, s5
	s_sext_i32_i8 s2, s2
	s_add_i32 s7, s4, s2
	s_ashr_i32 s60, s5, 3
	s_mov_b64 s[4:5], -1

;     __device__ __forceinline__ bool next(int i, Unit& u) const {
;         const int L = i * G + c; const int n0 = nM0 * nN0;
;         if (L < n0) { tile_map(L, nM0, nN0, u.pm, u.pn); u.g = -1; u.kt0 = 0; u.nt = ntK; }
;         else { const int l2 = L - n0; if (l2 >= nM1 * nN1 * ksplit) return false; int a, b; const int part = l2 % ksplit; tile_map(l2 / ksplit, nM1, nN1, a, b); u.pm = pm1 + a; u.pn = pn1 + b;
;             if (ksplit > 1) { u.g = part; u.nt = ntK / ksplit; u.kt0 = part * u.nt; } else { u.g = -1; u.kt0 = 0; u.nt = ntK; } }
.LBB0_1746:
	s_add_i32 s77, s77, 1
	s_mul_i32 s55, s77, s99
	s_add_i32 s55, s55, s98
	s_cmpk_gt_i32 s55, 0x33f
	s_cbranch_scc0 .LBB0_1849
	s_add_i32 s58, s55, 0xfffffcc0
	s_cmp_gt_u32 s58, 11
	s_mov_b64 s[56:57], -1
	s_cbranch_scc0 .LBB0_1850
	s_lshl_b32 s64, s97, 8
	s_mov_b64 s[6:7], 0
	s_mov_b64 s[56:57], 0
	s_cbranch_execz .LBB0_1851
